# baseline (speedup 1.0000x reference)
.Lmy_nonp6:
	s_and_b64 vcc, exec, s[30:31]
	s_cbranch_vccz .LBB1_43
	s_load_dwordx2 s[0:1], s[0:1], 0x68
	v_mov_b32_e32 v99, 0
	v_lshl_or_b32 v65, s42, 1, v115
	s_waitcnt lgkmcnt(0)
	s_add_u32 s8, s0, s33
	s_addc_u32 s9, s1, 0
	global_load_dwordx4 v[2:5], v98, s[8:9]
	s_movk_i32 s0, 0x1000
	v_lshl_add_u64 v[126:127], s[8:9], 0, v[98:99]
	v_add_co_u32_e32 v10, vcc, s0, v126
	v_cmp_gt_u32_e64 s[0:1], 21, v114
	s_nop 0
	v_addc_co_u32_e32 v11, vcc, 0, v127, vcc
	global_load_dwordx4 v[6:9], v[10:11], off offset:2048
	global_load_dwordx4 v[34:37], v[10:11], off
	global_load_dwordx4 v[54:57], v[10:11], off offset:3072
	v_cndmask_b32_e64 v64, 20, v114, s[0:1]
	s_movk_i32 s7, 0x150
	v_lshlrev_b32_e32 v71, 4, v65
	v_mad_u64_u32 v[12:13], s[12:13], v65, s7, v[64:65]
	v_mov_b32_e32 v13, v99
	v_or_b32_e32 v70, 1, v71
	v_lshlrev_b64 v[12:13], 2, v[12:13]
	v_mad_u64_u32 v[86:87], s[12:13], v70, 21, v[64:65]
	v_lshlrev_b32_e32 v73, 2, v64
	v_lshl_add_u64 v[14:15], s[50:51], 0, v[12:13]
	v_lshl_add_u64 v[12:13], s[36:37], 0, v[12:13]
	v_mov_b32_e32 v87, v99
	global_load_dword v81, v73, s[44:45]
	global_load_dword v62, v73, s[46:47]
	global_load_dword v83, v73, s[48:49]
	global_load_dword v69, v73, s[38:39]
	global_load_dword v63, v73, s[40:41]
	global_load_dword v75, v[14:15], off
	global_load_dword v72, v[12:13], off
	v_lshlrev_b64 v[12:13], 2, v[86:87]
	v_lshl_add_u64 v[14:15], s[50:51], 0, v[12:13]
	v_lshl_add_u64 v[12:13], s[36:37], 0, v[12:13]
	global_load_dwordx4 v[50:53], v98, s[8:9] offset:1024
	global_load_dword v76, v[14:15], off
	global_load_dword v74, v[12:13], off
	global_load_dwordx4 v[58:61], v[10:11], off offset:1024
	global_load_dwordx4 v[118:121], v[126:127], off offset:2048
	global_load_dwordx4 v[122:125], v[126:127], off offset:3072
	v_add_u32_e32 v98, 21, v86
	v_lshlrev_b64 v[12:13], 2, v[98:99]
	v_lshl_add_u64 v[10:11], s[50:51], 0, v[12:13]
	v_lshl_add_u64 v[12:13], s[36:37], 0, v[12:13]
	global_load_dword v105, v[10:11], off
	global_load_dword v77, v[12:13], off
	v_add_u32_e32 v98, 42, v86
	v_lshlrev_b64 v[14:15], 2, v[98:99]
	v_lshl_add_u64 v[10:11], s[50:51], 0, v[14:15]
	v_lshl_add_u64 v[12:13], s[36:37], 0, v[14:15]
	global_load_dword v106, v[10:11], off
	global_load_dword v78, v[12:13], off
	v_add_u32_e32 v98, 63, v86
	v_lshlrev_b64 v[14:15], 2, v[98:99]
	v_lshl_add_u64 v[10:11], s[50:51], 0, v[14:15]
	v_lshl_add_u64 v[12:13], s[36:37], 0, v[14:15]
	global_load_dword v107, v[10:11], off
	global_load_dword v79, v[12:13], off
	v_add_u32_e32 v98, 0x54, v86
	v_or_b32_e32 v68, 10, v71
	v_lshlrev_b64 v[126:127], 2, v[98:99]
	v_lshl_add_u64 v[42:43], s[50:51], 0, v[126:127]
	v_lshl_add_u64 v[44:45], s[36:37], 0, v[126:127]
	global_load_dword v108, v[42:43], off
	global_load_dword v102, v[44:45], off
	v_add_u32_e32 v98, 0x69, v86
	v_lshlrev_b64 v[46:47], 2, v[98:99]
	v_lshl_add_u64 v[84:85], s[50:51], 0, v[46:47]
	v_lshl_add_u64 v[88:89], s[36:37], 0, v[46:47]
	global_load_dword v109, v[84:85], off
	global_load_dword v103, v[88:89], off
	v_add_u32_e32 v98, 0x7e, v86
	v_lshlrev_b64 v[90:91], 2, v[98:99]
	v_lshl_add_u64 v[84:85], s[50:51], 0, v[90:91]
	v_lshl_add_u64 v[88:89], s[36:37], 0, v[90:91]
	global_load_dword v104, v[84:85], off
	global_load_dword v101, v[88:89], off
	v_add_u32_e32 v98, 0x93, v86
	v_lshlrev_b64 v[90:91], 2, v[98:99]
	v_add_u32_e32 v98, 0xa8, v86
	v_lshl_add_u64 v[42:43], s[50:51], 0, v[90:91]
	global_load_dword v100, v[42:43], off
	v_lshl_add_u64 v[42:43], s[36:37], 0, v[90:91]
	global_load_dword v84, v[42:43], off
	v_lshlrev_b64 v[42:43], 2, v[98:99]
	v_lshl_add_u64 v[44:45], s[50:51], 0, v[42:43]
	global_load_dword v98, v[44:45], off
	v_lshl_add_u64 v[42:43], s[36:37], 0, v[42:43]
	global_load_dword v85, v[42:43], off
	v_min_u32_e32 v42, 0x79, v68
	v_mul_u32_u24_e32 v42, 21, v42
	v_add_lshl_u32 v42, v42, v64, 2
	v_or_b32_e32 v43, 11, v71
	global_load_dword v97, v42, s[50:51]
	global_load_dword v86, v42, s[36:37]
	v_min_u32_e32 v42, 0x79, v43
	v_mul_u32_u24_e32 v42, 21, v42
	v_add_lshl_u32 v42, v42, v64, 2
	v_or_b32_e32 v44, 12, v71
	global_load_dword v96, v42, s[50:51]
	global_load_dword v87, v42, s[36:37]
	v_min_u32_e32 v42, 0x79, v44
	v_mul_u32_u24_e32 v42, 21, v42
	v_add_lshl_u32 v42, v42, v64, 2
	v_or_b32_e32 v45, 13, v71
	global_load_dword v95, v42, s[50:51]
	global_load_dword v92, v42, s[36:37]
	v_min_u32_e32 v42, 0x79, v45
	v_mul_u32_u24_e32 v42, 21, v42
	v_add_lshl_u32 v42, v42, v64, 2
	global_load_dword v93, v42, s[50:51]
	global_load_dword v89, v42, s[36:37]
	v_or_b32_e32 v42, 14, v71
	v_or_b32_e32 v46, 15, v71
	v_min_u32_e32 v80, 0x79, v42
	v_min_u32_e32 v47, 0x79, v46
	v_mul_u32_u24_e32 v80, 21, v80
	v_mul_u32_u24_e32 v47, 21, v47
	v_add_lshl_u32 v80, v80, v64, 2
	v_add_lshl_u32 v47, v47, v64, 2
	global_load_dword v94, v80, s[50:51]
	global_load_dword v90, v80, s[36:37]
	global_load_dword v91, v47, s[50:51]
	global_load_dword v88, v47, s[36:37]
	s_branch .LBB1_43
